# top-k unit layer-3 copy: second half-key weight fragments issued with the first half's loads
# speedup vs baseline: 1.0141x; 1.0017x over previous
.LBB0_977:
	s_or_b64 exec, exec, s[18:19]
	s_lshl_b32 s18, s28, 16
	v_readlane_b32 s19, v255, 18
	v_and_b32_e32 v10, 15, v2
	s_or_b32 s18, s18, s19
	v_readlane_b32 s19, v255, 4
	v_or_b32_e32 v0, s61, v10
	s_add_u32 s18, s19, s18
	v_readlane_b32 s19, v255, 12
	v_ashrrev_i32_e32 v1, 31, v0
	s_addc_u32 s19, s19, 0
	v_lshlrev_b64 v[0:1], 8, v[0:1]
	v_lshl_add_u64 v[0:1], s[18:19], 0, v[0:1]
	v_and_b32_e32 v104, 48, v2
	v_and_b32_e32 v20, 63, v2
	v_lshl_add_u64 v[0:1], v[0:1], 0, v[104:105]
	v_lshrrev_b32_e32 v2, 2, v2
	s_waitcnt lgkmcnt(0)
	s_barrier
	v_and_b32_e32 v11, 12, v2
	global_load_dwordx4 v[2:5], v[0:1], off
	global_load_dwordx4 v[6:9], v[0:1], off offset:64
	global_load_dwordx4 v[24:27], v[0:1], off offset:128
	global_load_dwordx4 v[28:31], v[0:1], off offset:192
	s_mov_b64 s[70:71], 0x8000
	v_lshl_add_u64 v[134:135], v[0:1], 0, s[70:71]
	global_load_dwordx4 v[136:139], v[134:135], off
	global_load_dwordx4 v[140:143], v[134:135], off offset:64
	global_load_dwordx4 v[146:149], v[134:135], off offset:128
	global_load_dwordx4 v[150:153], v[134:135], off offset:192
	v_lshl_add_u32 v23, v10, 2, v16
	v_mul_u32_u24_e32 v10, 0x210, v10
	v_add3_u32 v21, v12, v104, v10
	ds_read_b128 v[32:35], v21
	ds_read_b128 v[36:39], v21 offset:64
	s_movk_i32 s18, 0x404
	v_mad_u32_u24 v22, v11, s18, v23
	v_mov_b32_e32 v10, 0x8080
	v_add_u32_e32 v40, 0x8400, v23
	v_mad_u32_u24 v44, v11, s18, v198
	s_mov_b32 s19, 0x8000
	v_add_u32_e32 v23, 0x8600, v23
	s_waitcnt vmcnt(7) lgkmcnt(1)
	v_mfma_f32_16x16x32_bf16 v[32:35], v[32:35], v[2:5], 0
	s_waitcnt vmcnt(6) lgkmcnt(0)
	v_mfma_f32_16x16x32_bf16 v[32:35], v[36:39], v[6:9], v[32:35]
	ds_read_b128 v[36:39], v21 offset:128
	s_waitcnt vmcnt(5) lgkmcnt(0)
	v_mfma_f32_16x16x32_bf16 v[32:35], v[36:39], v[24:27], v[32:35]
	ds_read_b128 v[36:39], v21 offset:192
	s_waitcnt vmcnt(4) lgkmcnt(0)
	v_mfma_f32_16x16x32_bf16 v[32:35], v[36:39], v[28:31], v[32:35]
	s_nop 7
	ds_write_b32 v22, v32 offset:33792
	ds_write_b32 v22, v33 offset:34820
	ds_write_b32 v22, v34 offset:35848
	ds_write_b32 v22, v35 offset:36876
	ds_read_b128 v[32:35], v21 offset:8448
	ds_read_b128 v[36:39], v21 offset:8512
	s_waitcnt lgkmcnt(1)
	v_mfma_f32_16x16x32_bf16 v[32:35], v[32:35], v[2:5], 0
	s_waitcnt lgkmcnt(0)
	v_mfma_f32_16x16x32_bf16 v[32:35], v[36:39], v[6:9], v[32:35]
	ds_read_b128 v[36:39], v21 offset:8576
	s_waitcnt lgkmcnt(0)
	v_mfma_f32_16x16x32_bf16 v[32:35], v[36:39], v[24:27], v[32:35]
	ds_read_b128 v[36:39], v21 offset:8640
	s_waitcnt lgkmcnt(0)
	v_mfma_f32_16x16x32_bf16 v[32:35], v[36:39], v[28:31], v[32:35]
	s_nop 7
	ds_write_b32 v22, v32 offset:50240
	ds_write_b32 v22, v33 offset:51268
	ds_write_b32 v22, v34 offset:52296
	ds_write_b32 v22, v35 offset:53324
	ds_read_b128 v[32:35], v21 offset:16896
	ds_read_b128 v[36:39], v21 offset:16960
	s_waitcnt lgkmcnt(1)
	v_mfma_f32_16x16x32_bf16 v[32:35], v[32:35], v[2:5], 0
	s_waitcnt lgkmcnt(0)
	v_mfma_f32_16x16x32_bf16 v[32:35], v[36:39], v[6:9], v[32:35]
	ds_read_b128 v[36:39], v21 offset:17024
	s_waitcnt lgkmcnt(0)
	v_mfma_f32_16x16x32_bf16 v[32:35], v[36:39], v[24:27], v[32:35]
	ds_read_b128 v[36:39], v21 offset:17088
	s_waitcnt lgkmcnt(0)
	v_mfma_f32_16x16x32_bf16 v[32:35], v[36:39], v[28:31], v[32:35]
	v_mad_u32_u24 v36, v11, s18, v10
	v_add_u32_e32 v10, v40, v36
	s_nop 5
	ds_write_b32 v10, v32
	v_mov_b32_e32 v10, 0x8484
	v_mad_u32_u24 v37, v11, s18, v10
	v_add_u32_e32 v10, v40, v37
	ds_write_b32 v10, v33
	v_mov_b32_e32 v10, 0x8888
	v_mad_u32_u24 v38, v11, s18, v10
	v_add_u32_e32 v10, v40, v38
	ds_write_b32 v10, v34
	v_mov_b32_e32 v10, 0x8c8c
	v_mad_u32_u24 v39, v11, s18, v10
	v_add_u32_e32 v10, v40, v39
	ds_write_b32 v10, v35
	ds_read_b128 v[32:35], v21 offset:25344
	s_waitcnt lgkmcnt(0)
	v_mfma_f32_16x16x32_bf16 v[2:5], v[32:35], v[2:5], 0
	ds_read_b128 v[32:35], v21 offset:25408
	s_waitcnt lgkmcnt(0)
	v_mfma_f32_16x16x32_bf16 v[2:5], v[32:35], v[6:9], v[2:5]
	ds_read_b128 v[6:9], v21 offset:25472
	s_waitcnt lgkmcnt(0)
	v_mfma_f32_16x16x32_bf16 v[2:5], v[6:9], v[24:27], v[2:5]
	ds_read_b128 v[6:9], v21 offset:25536
	s_waitcnt lgkmcnt(0)
	v_mfma_f32_16x16x32_bf16 v[2:5], v[6:9], v[28:31], v[2:5]
	v_mov_b32_e32 v6, 0xc0c0
	v_mad_u32_u24 v41, v11, s18, v6
	v_add_u32_e32 v6, v40, v41
	s_nop 4
	ds_write_b32 v6, v2
	v_mov_b32_e32 v2, 0xc4c4
	v_mad_u32_u24 v42, v11, s18, v2
	v_add_u32_e32 v2, v40, v42
	ds_write_b32 v2, v3
	v_mov_b32_e32 v2, 0xc8c8
	v_mad_u32_u24 v43, v11, s18, v2
	v_add_u32_e32 v2, v40, v43
	ds_write_b32 v2, v4
	v_add_u32_e32 v2, v40, v44
	ds_write_b32 v2, v5
	s_nop 0
	ds_read_b128 v[28:31], v21 offset:256
	ds_read_b128 v[32:35], v21 offset:320
	s_waitcnt vmcnt(3) lgkmcnt(1)
	v_mfma_f32_16x16x32_bf16 v[28:31], v[28:31], v[136:139], 0
	s_waitcnt vmcnt(2) lgkmcnt(0)
	v_mfma_f32_16x16x32_bf16 v[28:31], v[32:35], v[140:143], v[28:31]
	ds_read_b128 v[32:35], v21 offset:384
	s_waitcnt vmcnt(1) lgkmcnt(0)
	v_mfma_f32_16x16x32_bf16 v[28:31], v[32:35], v[146:149], v[28:31]
	ds_read_b128 v[32:35], v21 offset:448
	s_waitcnt vmcnt(0) lgkmcnt(0)
	v_mfma_f32_16x16x32_bf16 v[28:31], v[32:35], v[150:153], v[28:31]
	s_nop 7
	ds_write_b32 v22, v28 offset:34304
	ds_write_b32 v22, v29 offset:35332
	ds_write_b32 v22, v30 offset:36360
	ds_write_b32 v22, v31 offset:37388
	ds_read_b128 v[28:31], v21 offset:8704
	ds_read_b128 v[32:35], v21 offset:8768
	s_waitcnt lgkmcnt(1)
	v_mfma_f32_16x16x32_bf16 v[28:31], v[28:31], v[136:139], 0
	s_waitcnt lgkmcnt(0)
	v_mfma_f32_16x16x32_bf16 v[28:31], v[32:35], v[140:143], v[28:31]
	ds_read_b128 v[32:35], v21 offset:8832
	s_waitcnt lgkmcnt(0)
	v_mfma_f32_16x16x32_bf16 v[28:31], v[32:35], v[146:149], v[28:31]
	ds_read_b128 v[32:35], v21 offset:8896
	s_waitcnt lgkmcnt(0)
	v_mfma_f32_16x16x32_bf16 v[28:31], v[32:35], v[150:153], v[28:31]
	s_nop 7
	ds_write_b32 v22, v28 offset:50752
	ds_write_b32 v22, v29 offset:51780
	ds_write_b32 v22, v30 offset:52808
	ds_write_b32 v22, v31 offset:53836
	ds_read_b128 v[28:31], v21 offset:17152
	ds_read_b128 v[32:35], v21 offset:17216
	s_waitcnt lgkmcnt(1)
	v_mfma_f32_16x16x32_bf16 v[28:31], v[28:31], v[136:139], 0
	v_add_u32_e32 v22, v23, v36
	s_waitcnt lgkmcnt(0)
	v_mfma_f32_16x16x32_bf16 v[28:31], v[32:35], v[140:143], v[28:31]
	ds_read_b128 v[32:35], v21 offset:17280
	s_waitcnt lgkmcnt(0)
	v_mfma_f32_16x16x32_bf16 v[28:31], v[32:35], v[146:149], v[28:31]
	ds_read_b128 v[32:35], v21 offset:17344
	s_waitcnt lgkmcnt(0)
	v_mfma_f32_16x16x32_bf16 v[28:31], v[32:35], v[150:153], v[28:31]
	s_nop 7
	ds_write_b32 v22, v28
	v_add_u32_e32 v22, v23, v37
	ds_write_b32 v22, v29
	v_add_u32_e32 v22, v23, v38
	ds_write_b32 v22, v30
	v_add_u32_e32 v22, v23, v39
	ds_write_b32 v22, v31
	ds_read_b128 v[28:31], v21 offset:25600
	s_waitcnt lgkmcnt(0)
	v_mfma_f32_16x16x32_bf16 v[4:7], v[28:31], v[136:139], 0
	ds_read_b128 v[28:31], v21 offset:25664
	s_waitcnt lgkmcnt(0)
	v_mfma_f32_16x16x32_bf16 v[0:3], v[28:31], v[140:143], v[4:7]
	s_nop 4
	ds_read_b128 v[4:7], v21 offset:25728
	s_waitcnt lgkmcnt(0)
	v_mfma_f32_16x16x32_bf16 v[0:3], v[4:7], v[146:149], v[0:3]
	ds_read_b128 v[4:7], v21 offset:25792
	v_mad_u32_u24 v10, v20, s18, v17
	v_readlane_b32 s18, v255, 19
	s_waitcnt lgkmcnt(0)
	v_mfma_f32_16x16x32_bf16 v[0:3], v[4:7], v[150:153], v[0:3]
	v_add_u32_e32 v4, v23, v41
	s_nop 6
	ds_write_b32 v4, v0
	v_add_u32_e32 v0, v23, v42
	ds_write_b32 v0, v1
	v_add_u32_e32 v0, v23, v43
	ds_write_b32 v0, v2
	v_add_u32_e32 v0, v23, v44
	ds_write_b32 v0, v3
	v_add_u32_e32 v0, 0x8400, v10
	s_waitcnt lgkmcnt(0)
	s_barrier
	ds_read2_b32 v[0:1], v0 offset1:1
	s_waitcnt lgkmcnt(0)
	v_not_b32_e32 v2, v0
	v_or_b32_e32 v3, 0x80000000, v0
	v_cmp_gt_i32_e32 vcc, 0, v0
	s_nop 1
	v_cndmask_b32_e32 v0, v3, v2, vcc
	v_and_b32_e32 v0, 0xffffff80, v0
	v_or_b32_e32 v6, s18, v0
	v_add_u32_e32 v0, 0x8440, v10
	ds_read2_b32 v[2:3], v0 offset1:1
	v_readlane_b32 s18, v255, 6
	s_waitcnt lgkmcnt(0)
	v_not_b32_e32 v0, v2
	v_or_b32_e32 v4, 0x80000000, v2
	v_cmp_gt_i32_e32 vcc, 0, v2
	v_or_b32_e32 v2, 0x80000000, v1
	s_nop 0
	v_cndmask_b32_e32 v0, v4, v0, vcc
	v_and_b32_e32 v0, 0xffffff80, v0
	v_or_b32_e32 v4, s18, v0
	v_not_b32_e32 v0, v1
	v_cmp_gt_i32_e32 vcc, 0, v1
	v_readlane_b32 s18, v255, 8
	v_or_b32_e32 v1, 0x80000000, v3
	v_cndmask_b32_e32 v0, v2, v0, vcc
	v_and_b32_e32 v0, 0xffffff80, v0
	v_or_b32_e32 v7, s18, v0
	v_not_b32_e32 v0, v3
	v_cmp_gt_i32_e32 vcc, 0, v3
	v_readlane_b32 s18, v255, 10
	s_nop 0
	v_cndmask_b32_e32 v0, v1, v0, vcc
	v_and_b32_e32 v0, 0xffffff80, v0
	v_or_b32_e32 v5, s18, v0
	v_add_u32_e32 v0, 0x8408, v10
	ds_read2_b32 v[0:1], v0 offset1:1
	v_readlane_b32 s18, v255, 14
	v_max_u32_e32 v49, v4, v5
	v_min_u32_e32 v4, v4, v5
	s_waitcnt lgkmcnt(0)
	v_not_b32_e32 v2, v0
	v_or_b32_e32 v3, 0x80000000, v0
	v_cmp_gt_i32_e32 vcc, 0, v0
	s_nop 1
	v_cndmask_b32_e32 v0, v3, v2, vcc
	v_and_b32_e32 v0, 0xffffff80, v0
	v_or_b32_e32 v11, s18, v0
	v_add_u32_e32 v0, 0x8448, v10
	ds_read2_b32 v[2:3], v0 offset1:1
	v_readlane_b32 s18, v255, 16
	s_waitcnt lgkmcnt(0)
	v_not_b32_e32 v0, v2
	v_or_b32_e32 v8, 0x80000000, v2
	v_cmp_gt_i32_e32 vcc, 0, v2
	v_or_b32_e32 v2, 0x80000000, v1
	s_nop 0
	v_cndmask_b32_e32 v0, v8, v0, vcc
	v_and_b32_e32 v0, 0xffffff80, v0
	v_or_b32_e32 v8, s18, v0
	v_not_b32_e32 v0, v1
	v_cmp_gt_i32_e32 vcc, 0, v1
	v_readlane_b32 s18, v255, 23
	v_or_b32_e32 v1, 0x80000000, v3
	v_cndmask_b32_e32 v0, v2, v0, vcc
	v_and_b32_e32 v0, 0xffffff80, v0
	v_or_b32_e32 v23, s18, v0
	v_not_b32_e32 v0, v3
	v_cmp_gt_i32_e32 vcc, 0, v3
	v_readlane_b32 s18, v255, 24
	s_nop 0
	v_cndmask_b32_e32 v0, v1, v0, vcc
	v_and_b32_e32 v0, 0xffffff80, v0
	v_or_b32_e32 v9, s18, v0
	v_add_u32_e32 v0, 0x8410, v10
	ds_read2_b32 v[0:1], v0 offset1:1
	v_readlane_b32 s18, v255, 25
	v_max_u32_e32 v5, v8, v9
	v_min_u32_e32 v8, v8, v9
	s_waitcnt lgkmcnt(0)
	v_not_b32_e32 v2, v0
	v_or_b32_e32 v3, 0x80000000, v0
	v_cmp_gt_i32_e32 vcc, 0, v0
	s_nop 1
	v_cndmask_b32_e32 v0, v3, v2, vcc
	v_and_b32_e32 v0, 0xffffff80, v0
	v_or_b32_e32 v24, s18, v0
	v_add_u32_e32 v0, 0x8450, v10
	ds_read2_b32 v[2:3], v0 offset1:1
	v_readlane_b32 s18, v255, 26
	s_waitcnt lgkmcnt(0)
	v_not_b32_e32 v0, v2
	v_or_b32_e32 v21, 0x80000000, v2
	v_cmp_gt_i32_e32 vcc, 0, v2
	v_or_b32_e32 v2, 0x80000000, v1
	s_nop 0
	v_cndmask_b32_e32 v0, v21, v0, vcc
	v_and_b32_e32 v0, 0xffffff80, v0
	v_or_b32_e32 v21, s18, v0
	v_not_b32_e32 v0, v1
	v_cmp_gt_i32_e32 vcc, 0, v1
	v_readlane_b32 s18, v255, 27
	v_or_b32_e32 v1, 0x80000000, v3
	v_cndmask_b32_e32 v0, v2, v0, vcc
	v_and_b32_e32 v0, 0xffffff80, v0
	v_or_b32_e32 v27, s18, v0
	v_not_b32_e32 v0, v3
	v_cmp_gt_i32_e32 vcc, 0, v3
	v_readlane_b32 s18, v255, 28
	s_nop 0
	v_cndmask_b32_e32 v0, v1, v0, vcc
	v_and_b32_e32 v0, 0xffffff80, v0
	v_or_b32_e32 v22, s18, v0
	v_add_u32_e32 v0, 0x8418, v10
	ds_read2_b32 v[0:1], v0 offset1:1
	v_readlane_b32 s18, v255, 29
	v_max_u32_e32 v9, v21, v22
	v_min_u32_e32 v21, v21, v22
	s_waitcnt lgkmcnt(0)
	v_not_b32_e32 v2, v0
	v_or_b32_e32 v3, 0x80000000, v0
	v_cmp_gt_i32_e32 vcc, 0, v0
	s_nop 1
	v_cndmask_b32_e32 v0, v3, v2, vcc
	v_and_b32_e32 v0, 0xffffff80, v0
	v_or_b32_e32 v28, s18, v0
	v_add_u32_e32 v0, 0x8458, v10
	ds_read2_b32 v[2:3], v0 offset1:1
	v_readlane_b32 s18, v255, 30
	s_waitcnt lgkmcnt(0)
	v_not_b32_e32 v0, v2
	v_or_b32_e32 v25, 0x80000000, v2
	v_cmp_gt_i32_e32 vcc, 0, v2
	v_or_b32_e32 v2, 0x80000000, v1
	s_nop 0
	v_cndmask_b32_e32 v0, v25, v0, vcc
	v_and_b32_e32 v0, 0xffffff80, v0
	v_or_b32_e32 v25, s18, v0
	v_not_b32_e32 v0, v1
	v_cmp_gt_i32_e32 vcc, 0, v1
	v_readlane_b32 s18, v255, 31
	v_or_b32_e32 v1, 0x80000000, v3
	v_cndmask_b32_e32 v0, v2, v0, vcc
	v_and_b32_e32 v0, 0xffffff80, v0
	v_or_b32_e32 v31, s18, v0
	v_not_b32_e32 v0, v3
	v_cmp_gt_i32_e32 vcc, 0, v3
	v_readlane_b32 s18, v255, 32
	s_nop 0
	v_cndmask_b32_e32 v0, v1, v0, vcc
	v_and_b32_e32 v0, 0xffffff80, v0
	v_or_b32_e32 v26, s56, v0
	v_add_u32_e32 v0, 0x8420, v10
	ds_read2_b32 v[0:1], v0 offset1:1
	v_max_u32_e32 v22, v25, v26
	v_min_u32_e32 v25, v25, v26
	s_waitcnt lgkmcnt(0)
	v_not_b32_e32 v2, v0
	v_or_b32_e32 v3, 0x80000000, v0
	v_cmp_gt_i32_e32 vcc, 0, v0
	s_nop 1
	v_cndmask_b32_e32 v0, v3, v2, vcc
	v_and_b32_e32 v0, 0xffffff80, v0
	v_or_b32_e32 v32, s18, v0
	v_add_u32_e32 v0, 0x8460, v10
	ds_read2_b32 v[2:3], v0 offset1:1
	s_movk_i32 s18, 0x800
	s_waitcnt lgkmcnt(0)
	v_not_b32_e32 v0, v2
	v_or_b32_e32 v29, 0x80000000, v2
	v_cmp_gt_i32_e32 vcc, 0, v2
	v_or_b32_e32 v2, 0x80000000, v1
	s_nop 0
	v_cndmask_b32_e32 v0, v29, v0, vcc
	v_and_b32_e32 v0, 0xffffff80, v0
	v_or_b32_e32 v29, s85, v0
	v_not_b32_e32 v0, v1
	v_cmp_gt_i32_e32 vcc, 0, v1
	v_or_b32_e32 v1, 0x80000000, v3
	s_nop 0
	v_cndmask_b32_e32 v0, v2, v0, vcc
	v_and_b32_e32 v0, 0xffffff80, v0
	v_or_b32_e32 v33, s49, v0
	v_not_b32_e32 v0, v3
	v_cmp_gt_i32_e32 vcc, 0, v3
	s_nop 1
	v_cndmask_b32_e32 v0, v1, v0, vcc
	v_and_b32_e32 v0, 0xffffff80, v0
	v_or_b32_e32 v30, s60, v0
	v_add_u32_e32 v0, 0x8428, v10
	ds_read2_b32 v[0:1], v0 offset1:1
	v_max_u32_e32 v26, v29, v30
	v_min_u32_e32 v29, v29, v30
	s_waitcnt lgkmcnt(0)
	v_not_b32_e32 v2, v0
	v_or_b32_e32 v3, 0x80000000, v0
	v_cmp_gt_i32_e32 vcc, 0, v0
	s_nop 1
	v_cndmask_b32_e32 v0, v3, v2, vcc
	v_add_u32_e32 v2, 0x8468, v10
	ds_read2_b32 v[2:3], v2 offset1:1
	v_and_b32_e32 v0, 0xffffff80, v0
	v_or_b32_e32 v0, s62, v0
	s_waitcnt lgkmcnt(0)
	v_not_b32_e32 v34, v2
	v_or_b32_e32 v35, 0x80000000, v2
	v_cmp_gt_i32_e32 vcc, 0, v2
	s_nop 1
	v_cndmask_b32_e32 v2, v35, v34, vcc
	v_and_b32_e32 v2, 0xffffff80, v2
	v_or_b32_e32 v36, s63, v2
	v_not_b32_e32 v2, v1
	v_or_b32_e32 v34, 0x80000000, v1
	v_cmp_gt_i32_e32 vcc, 0, v1
	s_nop 1
	v_cndmask_b32_e32 v1, v34, v2, vcc
	v_not_b32_e32 v2, v3
	v_or_b32_e32 v34, 0x80000000, v3
	v_cmp_gt_i32_e32 vcc, 0, v3
	v_and_b32_e32 v1, 0xffffff80, v1
	v_or_b32_e32 v1, s64, v1
	v_cndmask_b32_e32 v2, v34, v2, vcc
	v_and_b32_e32 v2, 0xffffff80, v2
	v_or_b32_e32 v37, s65, v2
	v_add_u32_e32 v2, 0x8430, v10
	ds_read2_b32 v[2:3], v2 offset1:1
	v_max_u32_e32 v30, v36, v37
	v_min_u32_e32 v36, v36, v37
	s_waitcnt lgkmcnt(0)
	v_not_b32_e32 v34, v2
	v_or_b32_e32 v35, 0x80000000, v2
	v_cmp_gt_i32_e32 vcc, 0, v2
	s_nop 1
	v_cndmask_b32_e32 v2, v35, v34, vcc
	v_and_b32_e32 v2, 0xffffff80, v2
	v_or_b32_e32 v38, s66, v2
	v_add_u32_e32 v2, 0x8470, v10
	ds_read2_b32 v[34:35], v2 offset1:1
	s_waitcnt lgkmcnt(0)
	v_not_b32_e32 v2, v34
	v_or_b32_e32 v39, 0x80000000, v34
	v_cmp_gt_i32_e32 vcc, 0, v34
	v_or_b32_e32 v34, 0x80000000, v3
	s_nop 0
	v_cndmask_b32_e32 v2, v39, v2, vcc
	v_and_b32_e32 v2, 0xffffff80, v2
	v_or_b32_e32 v39, s67, v2
	v_not_b32_e32 v2, v3
	v_cmp_gt_i32_e32 vcc, 0, v3
	v_or_b32_e32 v3, 0x80000000, v35
	s_nop 0
	v_cndmask_b32_e32 v2, v34, v2, vcc
	v_and_b32_e32 v2, 0xffffff80, v2
	v_or_b32_e32 v40, s42, v2
	v_not_b32_e32 v2, v35
	v_cmp_gt_i32_e32 vcc, 0, v35
	s_nop 1
	v_cndmask_b32_e32 v2, v3, v2, vcc
	v_and_b32_e32 v2, 0xffffff80, v2
	v_or_b32_e32 v41, s96, v2
	v_add_u32_e32 v2, 0x8438, v10
	ds_read2_b32 v[2:3], v2 offset1:1
	v_add_u32_e32 v10, 0x8478, v10
	v_max_u32_e32 v37, v39, v41
	v_min_u32_e32 v39, v39, v41
	s_waitcnt lgkmcnt(0)
	v_not_b32_e32 v34, v2
	v_or_b32_e32 v35, 0x80000000, v2
	v_cmp_gt_i32_e32 vcc, 0, v2
	s_nop 1
	v_cndmask_b32_e32 v2, v35, v34, vcc
	ds_read2_b32 v[34:35], v10 offset1:1
	v_and_b32_e32 v2, 0xffffff80, v2
	v_or_b32_e32 v2, s97, v2
	s_waitcnt lgkmcnt(0)
	v_not_b32_e32 v10, v34
	v_or_b32_e32 v42, 0x80000000, v34
	v_cmp_gt_i32_e32 vcc, 0, v34
	v_not_b32_e32 v34, v3
	s_nop 0
	v_cndmask_b32_e32 v10, v42, v10, vcc
	v_or_b32_e32 v42, 0x80000000, v3
	v_cmp_gt_i32_e32 vcc, 0, v3
	v_and_b32_e32 v10, 0xffffff80, v10
	v_or_b32_e32 v10, s45, v10
	v_cndmask_b32_e32 v3, v42, v34, vcc
	v_not_b32_e32 v34, v35
	v_or_b32_e32 v42, 0x80000000, v35
	v_cmp_gt_i32_e32 vcc, 0, v35
	v_and_b32_e32 v3, 0xffffff80, v3
	v_or_b32_e32 v3, s53, v3
	v_cndmask_b32_e32 v34, v42, v34, vcc
	v_and_b32_e32 v34, 0xffffff80, v34
	v_or_b32_e32 v34, s24, v34
	v_max_u32_e32 v35, v6, v7
	v_min_u32_e32 v6, v6, v7
	v_max_u32_e32 v7, v11, v23
	v_min_u32_e32 v11, v11, v23
	v_max_u32_e32 v23, v24, v27
	v_min_u32_e32 v24, v24, v27
	v_max_u32_e32 v27, v28, v31
	v_min_u32_e32 v28, v28, v31
	v_max_u32_e32 v31, v32, v33
	v_min_u32_e32 v32, v32, v33
	v_max_u32_e32 v33, v0, v1
	v_min_u32_e32 v0, v0, v1
	v_max_u32_e32 v1, v38, v40
	v_min_u32_e32 v38, v38, v40
	v_max_u32_e32 v40, v2, v3
	v_min_u32_e32 v2, v2, v3
	v_max_u32_e32 v41, v10, v34
	v_min_u32_e32 v10, v10, v34
	v_max_u32_e32 v3, v35, v11
	v_min_u32_e32 v11, v35, v11
	v_max_u32_e32 v35, v6, v7
	v_min_u32_e32 v6, v6, v7
	v_max_u32_e32 v7, v23, v28
	v_min_u32_e32 v23, v23, v28
	v_max_u32_e32 v28, v24, v27
	v_min_u32_e32 v24, v24, v27
	v_max_u32_e32 v27, v31, v0
	v_min_u32_e32 v0, v31, v0
	v_max_u32_e32 v31, v32, v33
	v_min_u32_e32 v32, v32, v33
	v_max_u32_e32 v33, v1, v2
	v_min_u32_e32 v1, v1, v2
	v_max_u32_e32 v2, v38, v40
	v_min_u32_e32 v38, v38, v40
	v_max_u32_e32 v34, v49, v8
	v_min_u32_e32 v8, v49, v8
	v_max_u32_e32 v49, v4, v5
	v_min_u32_e32 v4, v4, v5
	v_max_u32_e32 v5, v9, v25
	v_min_u32_e32 v9, v9, v25
	v_max_u32_e32 v25, v21, v22
	v_min_u32_e32 v21, v21, v22
	v_max_u32_e32 v22, v26, v36
	v_min_u32_e32 v26, v26, v36
	v_max_u32_e32 v36, v29, v30
	v_min_u32_e32 v29, v29, v30
	v_max_u32_e32 v30, v37, v10
	v_min_u32_e32 v10, v37, v10
	v_max_u32_e32 v37, v39, v41
	v_min_u32_e32 v39, v39, v41
	v_max_u32_e32 v40, v3, v35
	v_min_u32_e32 v3, v3, v35
	v_max_u32_e32 v35, v11, v6
	v_min_u32_e32 v6, v11, v6
	v_max_u32_e32 v11, v23, v24
	v_min_u32_e32 v23, v23, v24
	v_max_u32_e32 v24, v7, v28
	v_min_u32_e32 v7, v7, v28
	v_max_u32_e32 v28, v27, v31
	v_min_u32_e32 v27, v27, v31
	v_max_u32_e32 v31, v0, v32
	v_min_u32_e32 v0, v0, v32
	v_max_u32_e32 v32, v1, v38
	v_min_u32_e32 v1, v1, v38
	v_max_u32_e32 v38, v33, v2
	v_min_u32_e32 v2, v33, v2
	v_max_u32_e32 v41, v34, v49
	v_min_u32_e32 v34, v34, v49
	v_max_u32_e32 v49, v8, v4
	v_min_u32_e32 v4, v8, v4
	v_max_u32_e32 v8, v9, v21
	v_min_u32_e32 v9, v9, v21
	v_max_u32_e32 v21, v5, v25
	v_min_u32_e32 v5, v5, v25
	v_max_u32_e32 v25, v22, v36
	v_min_u32_e32 v22, v22, v36
	v_max_u32_e32 v36, v26, v29
	v_min_u32_e32 v26, v26, v29
	v_max_u32_e32 v29, v10, v39
	v_min_u32_e32 v10, v10, v39
	v_max_u32_e32 v39, v30, v37
	v_min_u32_e32 v30, v30, v37
	v_max_u32_e32 v33, v40, v23
	v_min_u32_e32 v23, v40, v23
	v_max_u32_e32 v40, v3, v11
	v_min_u32_e32 v3, v3, v11
	v_max_u32_e32 v11, v35, v7
	v_min_u32_e32 v7, v35, v7
	v_max_u32_e32 v35, v6, v24
	v_min_u32_e32 v6, v6, v24
	v_max_u32_e32 v24, v28, v1
	v_min_u32_e32 v1, v28, v1
	v_max_u32_e32 v28, v27, v32
	v_min_u32_e32 v27, v27, v32
	v_max_u32_e32 v32, v31, v2
	v_min_u32_e32 v2, v31, v2
	v_max_u32_e32 v31, v0, v38
	v_min_u32_e32 v0, v0, v38
	v_max_u32_e32 v37, v41, v9
	v_min_u32_e32 v9, v41, v9
	v_max_u32_e32 v41, v34, v8
	v_min_u32_e32 v8, v34, v8
	v_max_u32_e32 v34, v49, v5
	v_min_u32_e32 v5, v49, v5
	v_max_u32_e32 v49, v4, v21
	v_min_u32_e32 v4, v4, v21
	v_max_u32_e32 v21, v25, v10
	v_min_u32_e32 v10, v25, v10
	v_max_u32_e32 v25, v22, v29
	v_min_u32_e32 v22, v22, v29
	v_max_u32_e32 v29, v36, v30
	v_min_u32_e32 v30, v36, v30
	v_max_u32_e32 v36, v26, v39
	v_min_u32_e32 v26, v26, v39
	v_max_u32_e32 v38, v33, v11
	v_min_u32_e32 v11, v33, v11
	v_max_u32_e32 v33, v40, v35
	v_min_u32_e32 v35, v40, v35
	v_max_u32_e32 v40, v23, v7
	v_min_u32_e32 v7, v23, v7
	v_max_u32_e32 v23, v3, v6
	v_min_u32_e32 v3, v3, v6
	v_max_u32_e32 v6, v1, v2
	v_min_u32_e32 v1, v1, v2
	v_max_u32_e32 v2, v27, v0
	v_min_u32_e32 v0, v27, v0
	v_max_u32_e32 v27, v24, v32
	v_min_u32_e32 v24, v24, v32
	v_max_u32_e32 v32, v28, v31
	v_min_u32_e32 v28, v28, v31
	v_max_u32_e32 v39, v37, v34
	v_min_u32_e32 v34, v37, v34
	v_max_u32_e32 v37, v41, v49
	v_min_u32_e32 v41, v41, v49
	v_max_u32_e32 v49, v9, v5
	v_min_u32_e32 v5, v9, v5
	v_max_u32_e32 v9, v8, v4
	v_min_u32_e32 v4, v8, v4
	v_max_u32_e32 v8, v10, v30
	v_min_u32_e32 v10, v10, v30
	v_max_u32_e32 v30, v22, v26
	v_min_u32_e32 v22, v22, v26
	v_max_u32_e32 v26, v21, v29
	v_min_u32_e32 v21, v21, v29
	v_max_u32_e32 v29, v25, v36
	v_min_u32_e32 v25, v25, v36
	v_max_u32_e32 v31, v38, v33
	v_min_u32_e32 v33, v38, v33
	v_max_u32_e32 v38, v11, v35
	v_min_u32_e32 v11, v11, v35
	v_max_u32_e32 v35, v40, v23
	v_min_u32_e32 v23, v40, v23
	v_max_u32_e32 v40, v7, v3
	v_min_u32_e32 v3, v7, v3
	v_max_u32_e32 v7, v1, v0
	v_min_u32_e32 v0, v1, v0
	v_max_u32_e32 v1, v6, v2
	v_min_u32_e32 v2, v6, v2
	v_max_u32_e32 v6, v24, v28
	v_min_u32_e32 v24, v24, v28
	v_max_u32_e32 v28, v27, v32
	v_min_u32_e32 v27, v27, v32
	v_max_u32_e32 v36, v39, v37
	v_min_u32_e32 v37, v39, v37
	v_max_u32_e32 v39, v34, v41
	v_min_u32_e32 v34, v34, v41
	v_max_u32_e32 v41, v49, v9
	v_min_u32_e32 v9, v49, v9
	v_max_u32_e32 v49, v5, v4
	v_min_u32_e32 v4, v5, v4
	v_max_u32_e32 v5, v10, v22
	v_min_u32_e32 v10, v10, v22
	v_max_u32_e32 v22, v8, v30
	v_min_u32_e32 v8, v8, v30
	v_max_u32_e32 v30, v21, v25
	v_min_u32_e32 v21, v21, v25
	v_max_u32_e32 v25, v26, v29
	v_min_u32_e32 v26, v26, v29
	v_max_u32_e32 v32, v31, v0
	v_min_u32_e32 v0, v31, v0
	v_max_u32_e32 v31, v33, v7
	v_min_u32_e32 v7, v33, v7
	v_max_u32_e32 v33, v38, v2
	v_min_u32_e32 v2, v38, v2
	v_max_u32_e32 v38, v11, v1
	v_min_u32_e32 v1, v11, v1
	v_max_u32_e32 v11, v35, v24
	v_min_u32_e32 v24, v35, v24
	v_max_u32_e32 v35, v23, v6
	v_min_u32_e32 v6, v23, v6
	v_max_u32_e32 v23, v40, v27
	v_min_u32_e32 v27, v40, v27
	v_max_u32_e32 v40, v3, v28
	v_min_u32_e32 v3, v3, v28
	v_max_u32_e32 v29, v36, v10
	v_min_u32_e32 v10, v36, v10
	v_max_u32_e32 v36, v37, v5
	v_min_u32_e32 v5, v37, v5
	v_max_u32_e32 v37, v39, v8
	v_min_u32_e32 v8, v39, v8
	v_max_u32_e32 v39, v34, v22
	v_min_u32_e32 v22, v34, v22
	v_max_u32_e32 v34, v41, v21
	v_min_u32_e32 v21, v41, v21
	v_max_u32_e32 v41, v9, v30
	v_min_u32_e32 v9, v9, v30
	v_max_u32_e32 v30, v49, v26
	v_min_u32_e32 v26, v49, v26
	v_max_u32_e32 v49, v4, v25
	v_min_u32_e32 v4, v4, v25
	v_max_u32_e32 v28, v32, v11
	v_min_u32_e32 v11, v32, v11
	v_max_u32_e32 v32, v31, v35
	v_min_u32_e32 v31, v31, v35
	v_max_u32_e32 v35, v33, v23
	v_min_u32_e32 v23, v33, v23
	v_max_u32_e32 v33, v38, v40
	v_min_u32_e32 v38, v38, v40
	v_max_u32_e32 v40, v0, v24
	v_min_u32_e32 v0, v0, v24
	v_max_u32_e32 v24, v7, v6
	v_min_u32_e32 v6, v7, v6
	v_max_u32_e32 v7, v2, v27
	v_min_u32_e32 v2, v2, v27
	v_max_u32_e32 v27, v1, v3
	v_min_u32_e32 v1, v1, v3
	v_max_u32_e32 v25, v29, v34
	v_min_u32_e32 v29, v29, v34
	v_max_u32_e32 v34, v36, v41
	v_min_u32_e32 v36, v36, v41
	v_max_u32_e32 v41, v37, v30
	v_min_u32_e32 v30, v37, v30
	v_max_u32_e32 v37, v39, v49
	v_min_u32_e32 v39, v39, v49
	v_max_u32_e32 v49, v10, v21
	v_min_u32_e32 v10, v10, v21
	v_max_u32_e32 v21, v5, v9
	v_min_u32_e32 v5, v5, v9
	v_max_u32_e32 v9, v8, v26
	v_min_u32_e32 v8, v8, v26
	v_max_u32_e32 v26, v22, v4
	v_min_u32_e32 v4, v22, v4
	v_max_u32_e32 v3, v28, v35
	v_min_u32_e32 v28, v28, v35
	v_max_u32_e32 v35, v32, v33
	v_min_u32_e32 v32, v32, v33
	v_max_u32_e32 v33, v11, v23
	v_min_u32_e32 v11, v11, v23
	v_max_u32_e32 v23, v31, v38
	v_min_u32_e32 v31, v31, v38
	v_max_u32_e32 v38, v40, v7
	v_min_u32_e32 v7, v40, v7
	v_max_u32_e32 v40, v24, v27
	v_min_u32_e32 v24, v24, v27
	v_max_u32_e32 v27, v0, v2
	v_min_u32_e32 v0, v0, v2
	v_max_u32_e32 v2, v6, v1
	v_min_u32_e32 v1, v6, v1
	v_max_u32_e32 v22, v25, v41
	v_min_u32_e32 v25, v25, v41
	v_max_u32_e32 v41, v34, v37
	v_min_u32_e32 v34, v34, v37
	v_max_u32_e32 v37, v29, v30
	v_min_u32_e32 v29, v29, v30
	v_max_u32_e32 v30, v36, v39
	v_min_u32_e32 v36, v36, v39
	v_max_u32_e32 v39, v49, v9
	v_min_u32_e32 v9, v49, v9
	v_max_u32_e32 v49, v21, v26
	v_min_u32_e32 v21, v21, v26
	v_max_u32_e32 v26, v10, v8
	v_min_u32_e32 v8, v10, v8
	v_max_u32_e32 v10, v5, v4
	v_min_u32_e32 v4, v5, v4
	v_min_u32_e32 v6, v3, v35
	v_min_u32_e32 v42, v28, v32
	v_min_u32_e32 v43, v33, v23
	v_min_u32_e32 v44, v11, v31
	v_min_u32_e32 v45, v38, v40
	v_min_u32_e32 v46, v7, v24
	v_min_u32_e32 v47, v27, v2
	v_min_u32_e32 v48, v0, v1
	v_min_u32_e32 v5, v22, v41
	v_min_u32_e32 v50, v25, v34
	v_min_u32_e32 v51, v37, v30
	v_min_u32_e32 v52, v29, v36
	v_min_u32_e32 v53, v39, v49
	v_min_u32_e32 v54, v9, v21
	v_min_u32_e32 v55, v26, v10
	v_min_u32_e32 v56, v8, v4
	v_max3_u32 v3, v3, v35, v56
	v_max3_u32 v4, v6, v8, v4
	v_max3_u32 v6, v28, v32, v55
	v_max3_u32 v8, v42, v26, v10
	v_max3_u32 v10, v33, v23, v54
	v_max3_u32 v9, v43, v9, v21
	v_max3_u32 v11, v11, v31, v53
	v_max3_u32 v21, v44, v39, v49
	v_max3_u32 v23, v38, v40, v52
	v_max3_u32 v26, v45, v29, v36
	v_max3_u32 v7, v7, v24, v51
	v_max3_u32 v24, v46, v37, v30
	v_max3_u32 v2, v27, v2, v50
	v_max3_u32 v25, v47, v25, v34
	v_max3_u32 v0, v0, v1, v5
	v_max3_u32 v1, v48, v22, v41
	v_max_u32_e32 v5, v3, v23
	v_min_u32_e32 v3, v3, v23
	v_max_u32_e32 v22, v4, v26
	v_min_u32_e32 v4, v4, v26
	v_max_u32_e32 v23, v6, v7
	v_min_u32_e32 v6, v6, v7
	v_max_u32_e32 v7, v8, v24
	v_min_u32_e32 v8, v8, v24
	v_max_u32_e32 v24, v10, v2
	v_min_u32_e32 v2, v10, v2
	v_max_u32_e32 v10, v9, v25
	v_min_u32_e32 v9, v9, v25
	v_max_u32_e32 v25, v11, v0
	v_min_u32_e32 v0, v11, v0
	v_max_u32_e32 v11, v21, v1
	v_min_u32_e32 v1, v21, v1
	v_max_u32_e32 v21, v5, v24
	v_min_u32_e32 v5, v5, v24
	v_max_u32_e32 v24, v22, v10
	v_min_u32_e32 v10, v22, v10
	v_max_u32_e32 v22, v23, v25
	v_min_u32_e32 v23, v23, v25
	v_max_u32_e32 v25, v7, v11
	v_min_u32_e32 v7, v7, v11
	v_max_u32_e32 v11, v3, v2
	v_min_u32_e32 v2, v3, v2
	v_max_u32_e32 v3, v4, v9
	v_min_u32_e32 v4, v4, v9
	v_max_u32_e32 v9, v6, v0
	v_min_u32_e32 v0, v6, v0
	v_max_u32_e32 v6, v8, v1
	v_min_u32_e32 v1, v8, v1
	v_max_u32_e32 v8, v21, v22
	v_min_u32_e32 v21, v21, v22
	v_max_u32_e32 v22, v24, v25
	v_min_u32_e32 v24, v24, v25
	v_max_u32_e32 v25, v5, v23
	v_min_u32_e32 v5, v5, v23
	v_max_u32_e32 v23, v10, v7
	v_min_u32_e32 v7, v10, v7
	v_max_u32_e32 v10, v11, v9
	v_min_u32_e32 v9, v11, v9
	v_max_u32_e32 v11, v3, v6
	v_min_u32_e32 v3, v3, v6
	v_max_u32_e32 v6, v2, v0
	v_min_u32_e32 v0, v2, v0
	v_max_u32_e32 v2, v4, v1
	v_min_u32_e32 v1, v4, v1
	v_mov_b32_e32 v43, s84
	v_max_u32_e32 v41, v0, v1
	v_min_u32_e32 v42, v0, v1
	v_bitop3_b32 v1, v20, s18, v43 bitop3:0x36
	v_max_u32_e32 v28, v8, v22
	v_min_u32_e32 v29, v8, v22
	v_lshl_add_u32 v0, v20, 2, v18
	v_lshl_add_u32 v1, v1, 2, v12
	v_max_u32_e32 v30, v21, v24
	v_min_u32_e32 v21, v21, v24
	v_max_u32_e32 v31, v25, v23
	v_min_u32_e32 v32, v25, v23
	v_max_u32_e32 v33, v5, v7
	v_min_u32_e32 v34, v5, v7
	v_max_u32_e32 v35, v10, v11
	v_min_u32_e32 v36, v10, v11
	v_max_u32_e32 v37, v9, v3
	v_min_u32_e32 v38, v9, v3
	v_max_u32_e32 v39, v6, v2
	v_min_u32_e32 v40, v6, v2
	ds_write2st64_b32 v0, v28, v29 offset1:1
	ds_write2st64_b32 v0, v30, v21 offset0:2 offset1:3
	ds_write2st64_b32 v0, v31, v32 offset0:4 offset1:5
	ds_write2st64_b32 v0, v33, v34 offset0:6 offset1:7
	ds_write2st64_b32 v0, v35, v36 offset0:8 offset1:9
	ds_write2st64_b32 v0, v37, v38 offset0:10 offset1:11
	ds_write2st64_b32 v0, v39, v40 offset0:12 offset1:13
	ds_write2st64_b32 v0, v41, v42 offset0:14 offset1:15
	s_waitcnt lgkmcnt(0)
	s_barrier
	ds_read2st64_b32 v[2:3], v1 offset1:1
	ds_read2st64_b32 v[4:5], v1 offset0:2 offset1:3
	ds_read2st64_b32 v[6:7], v1 offset0:4 offset1:5
	ds_read2st64_b32 v[8:9], v1 offset0:6 offset1:7
	ds_read2st64_b32 v[10:11], v1 offset0:8 offset1:9
	ds_read2st64_b32 v[22:23], v1 offset0:10 offset1:11
	ds_read2st64_b32 v[24:25], v1 offset0:12 offset1:13
	ds_read2st64_b32 v[26:27], v1 offset0:14 offset1:15
	s_waitcnt lgkmcnt(4)
	v_max_u32_e32 v9, v35, v9
	s_waitcnt lgkmcnt(3)
	v_max_u32_e32 v11, v33, v11
	s_waitcnt lgkmcnt(2)
	v_max_u32_e32 v23, v31, v23
	s_waitcnt lgkmcnt(1)
	v_max_u32_e32 v25, v30, v25
	s_waitcnt lgkmcnt(0)
	v_max_u32_e32 v27, v28, v27
	v_max_u32_e32 v26, v29, v26
	v_max_u32_e32 v21, v21, v24
	v_max_u32_e32 v22, v32, v22
	v_max_u32_e32 v10, v34, v10
	v_max_u32_e32 v8, v36, v8
	v_max_u32_e32 v7, v37, v7
	v_max_u32_e32 v6, v38, v6
	v_max_u32_e32 v5, v39, v5
	v_max_u32_e32 v4, v40, v4
	v_max_u32_e32 v3, v41, v3
	v_max_u32_e32 v2, v42, v2
	v_max_u32_e32 v24, v27, v9
	v_min_u32_e32 v9, v27, v9
	v_max_u32_e32 v27, v26, v8
	v_min_u32_e32 v8, v26, v8
	v_max_u32_e32 v26, v25, v7
	v_min_u32_e32 v7, v25, v7
	v_max_u32_e32 v25, v21, v6
	v_min_u32_e32 v6, v21, v6
	v_max_u32_e32 v21, v23, v5
	v_min_u32_e32 v5, v23, v5
	v_max_u32_e32 v23, v22, v4
	v_min_u32_e32 v4, v22, v4
	v_max_u32_e32 v22, v11, v3
	v_min_u32_e32 v3, v11, v3
	v_max_u32_e32 v11, v10, v2
	v_min_u32_e32 v2, v10, v2
	v_max_u32_e32 v10, v24, v21
	v_min_u32_e32 v21, v24, v21
	v_max_u32_e32 v24, v27, v23
	v_min_u32_e32 v23, v27, v23
	v_max_u32_e32 v27, v26, v22
	v_min_u32_e32 v22, v26, v22
	v_max_u32_e32 v26, v25, v11
	v_min_u32_e32 v11, v25, v11
	v_max_u32_e32 v25, v9, v5
	v_min_u32_e32 v5, v9, v5
	v_max_u32_e32 v9, v8, v4
	v_min_u32_e32 v4, v8, v4
	v_max_u32_e32 v8, v7, v3
	v_min_u32_e32 v3, v7, v3
	v_max_u32_e32 v7, v6, v2
	v_min_u32_e32 v2, v6, v2
	v_max_u32_e32 v6, v10, v27
	v_min_u32_e32 v10, v10, v27
	v_max_u32_e32 v27, v24, v26
	v_min_u32_e32 v24, v24, v26
	v_max_u32_e32 v28, v21, v22
	v_min_u32_e32 v22, v21, v22
	v_max_u32_e32 v21, v23, v11
	v_min_u32_e32 v29, v23, v11
	v_max_u32_e32 v30, v25, v8
	v_min_u32_e32 v8, v25, v8
	v_max_u32_e32 v25, v9, v7
	v_min_u32_e32 v7, v9, v7
	v_min_u32_e32 v32, v5, v3
	v_max_u32_e32 v33, v4, v2
	v_min_u32_e32 v2, v4, v2
	s_movk_i32 s18, 0x1000
	v_max_u32_e32 v31, v5, v3
	v_max_u32_e32 v26, v6, v27
	v_min_u32_e32 v5, v6, v27
	v_max_u32_e32 v11, v10, v24
	v_min_u32_e32 v3, v10, v24
	v_max_u32_e32 v23, v28, v21
	v_min_u32_e32 v6, v28, v21
	v_max_u32_e32 v21, v22, v29
	v_min_u32_e32 v4, v22, v29
	v_max_u32_e32 v22, v8, v7
	v_min_u32_e32 v7, v8, v7
	v_max_u32_e32 v24, v32, v2
	v_min_u32_e32 v8, v32, v2
	v_bitop3_b32 v2, v20, s18, v43 bitop3:0x36
	v_max_u32_e32 v27, v30, v25
	v_min_u32_e32 v9, v30, v25
	v_max_u32_e32 v25, v31, v33
	v_min_u32_e32 v10, v31, v33
	v_lshl_add_u32 v2, v2, 2, v12
	s_and_b64 vcc, exec, s[34:35]
	ds_write2st64_b32 v0, v26, v5 offset0:132 offset1:133
	ds_write2st64_b32 v0, v11, v3 offset0:134 offset1:135
	ds_write2st64_b32 v0, v23, v6 offset0:136 offset1:137
	ds_write2st64_b32 v0, v21, v4 offset0:138 offset1:139
	ds_write2st64_b32 v0, v27, v9 offset0:140 offset1:141
	ds_write2st64_b32 v0, v22, v7 offset0:142 offset1:143
	ds_write2st64_b32 v0, v25, v10 offset0:144 offset1:145
	ds_write2st64_b32 v0, v24, v8 offset0:146 offset1:147
	s_waitcnt lgkmcnt(0)
	s_barrier
	s_cbranch_vccz .LBB0_979
	ds_read2st64_b32 v[28:29], v2 offset0:146 offset1:147
	ds_read2st64_b32 v[30:31], v2 offset0:138 offset1:139
	ds_read2st64_b32 v[32:33], v2 offset0:142 offset1:143
	ds_read2st64_b32 v[34:35], v2 offset0:144 offset1:145
	ds_read2st64_b32 v[36:37], v2 offset0:134 offset1:135
	ds_read2st64_b32 v[38:39], v2 offset0:136 offset1:137
	s_waitcnt lgkmcnt(5)
	v_max_u32_e32 v29, v26, v29
	s_waitcnt lgkmcnt(4)
	v_max_u32_e32 v31, v27, v31
	ds_read2st64_b32 v[26:27], v2 offset0:140 offset1:141
	ds_read2st64_b32 v[40:41], v2 offset0:132 offset1:133
	s_waitcnt lgkmcnt(5)
	v_max_u32_e32 v23, v23, v33
	s_waitcnt lgkmcnt(3)
	v_max_u32_e32 v25, v25, v37
	v_max_u32_e32 v11, v11, v35
	s_waitcnt lgkmcnt(2)
	v_max_u32_e32 v22, v22, v39
	s_waitcnt lgkmcnt(1)
	v_max_u32_e32 v21, v21, v27
	s_waitcnt lgkmcnt(0)
	v_max_u32_e32 v24, v24, v41
	v_max_u32_e32 v5, v5, v28
	v_max_u32_e32 v9, v9, v30
	v_max_u32_e32 v6, v6, v32
	v_max_u32_e32 v10, v10, v36
	v_max_u32_e32 v3, v3, v34
	v_max_u32_e32 v7, v7, v38
	v_max_u32_e32 v4, v4, v26
	v_max_u32_e32 v8, v8, v40
	v_min_u32_e32 v42, v29, v31
	v_min_u32_e32 v33, v23, v25
	v_min_u32_e32 v35, v11, v22
	v_min_u32_e32 v27, v21, v24
	v_min_u32_e32 v28, v5, v9
	v_min_u32_e32 v30, v6, v10
	v_min_u32_e32 v34, v3, v7
	v_min_u32_e32 v26, v4, v8
	v_min_u32_e32 v37, v42, v33
	v_min_u32_e32 v39, v35, v27
	v_min_u32_e32 v32, v28, v30
	v_min_u32_e32 v36, v34, v26
	v_max_u32_e32 v33, v42, v33
	v_max_u32_e32 v27, v35, v27
	v_max_u32_e32 v28, v28, v30
	v_max_u32_e32 v26, v34, v26
	v_min_u32_e32 v35, v33, v27
	v_min_u32_e32 v30, v28, v26
	v_max_u32_e32 v27, v33, v27
	v_max_u32_e32 v26, v28, v26
	v_min_u32_e32 v28, v27, v26
	v_max_u32_e32 v26, v27, v26
	v_max_u32_e32 v27, v29, v31
	v_max_u32_e32 v23, v23, v25
	v_max_u32_e32 v11, v11, v22
	v_max_u32_e32 v21, v21, v24
	v_max_u32_e32 v5, v5, v9
	v_max_u32_e32 v6, v6, v10
	v_max_u32_e32 v3, v3, v7
	v_max_u32_e32 v4, v4, v8
	v_min_u32_e32 v25, v27, v23
	v_min_u32_e32 v22, v11, v21
	v_min_u32_e32 v9, v5, v6
	v_min_u32_e32 v7, v3, v4
	v_min_u32_e32 v24, v25, v22
	v_min_u32_e32 v8, v9, v7
	v_max_u32_e32 v22, v25, v22
	v_max_u32_e32 v7, v9, v7
	v_min_u32_e32 v9, v22, v7
	v_max_u32_e32 v7, v22, v7
	v_max_u32_e32 v22, v27, v23
	v_max_u32_e32 v11, v11, v21
	v_max_u32_e32 v5, v5, v6
	v_max_u32_e32 v3, v3, v4
	v_min_u32_e32 v21, v22, v11
	v_min_u32_e32 v4, v5, v3
	v_max_u32_e32 v11, v22, v11
	v_max_u32_e32 v3, v5, v3
	v_min_u32_e32 v41, v37, v39
	v_min_u32_e32 v38, v32, v36
	v_max_u32_e32 v37, v37, v39
	v_max_u32_e32 v32, v32, v36
	v_min_u32_e32 v5, v11, v3
	v_max_u32_e32 v3, v11, v3
	v_lshl_add_u32 v11, v20, 2, v19
	v_min_u32_e32 v40, v41, v38
	v_max_u32_e32 v38, v41, v38
	v_min_u32_e32 v36, v37, v32
	v_max_u32_e32 v32, v37, v32
	v_min_u32_e32 v34, v35, v30
	v_max_u32_e32 v30, v35, v30
	v_min_u32_e32 v10, v24, v8
	v_max_u32_e32 v8, v24, v8
	v_min_u32_e32 v6, v21, v4
	v_max_u32_e32 v4, v21, v4
	ds_write2st64_b32 v11, v3, v5 offset1:1
	ds_write2st64_b32 v11, v4, v6 offset0:2 offset1:3
	ds_write2st64_b32 v11, v7, v9 offset0:4 offset1:5
	ds_write2st64_b32 v11, v8, v10 offset0:6 offset1:7
	ds_write2st64_b32 v11, v26, v28 offset0:8 offset1:9
	ds_write2st64_b32 v11, v30, v34 offset0:10 offset1:11
	ds_write2st64_b32 v11, v32, v36 offset0:12 offset1:13
	ds_write2st64_b32 v11, v38, v40 offset0:14 offset1:15
